# baseline (speedup 1.0000x reference)
_Z9nerf_mainPKfS0_S0_PKiS2_PKcS0_Pf:
	s_load_dwordx8 s[8:15], s[0:1], 0x20
	s_load_dwordx8 s[24:31], s[0:1], 0x0
	v_readfirstlane_b32 s3, v0
	v_and_b32_e32 v120, 63, v0
	v_lshlrev_b32_e32 v121, 4, v120
	s_getpc_b64 s[70:71]
	v_lshlrev_b32_e32 v190, 6, v0
	v_min_u32_e32 v190, 0x7700, v190
	global_load_dword v191, v190, s[70:71]
	s_mov_b32 s39, 0x20000
	s_waitcnt lgkmcnt(0)
	s_load_dword s50, s[30:31], 0x0
	s_load_dword s51, s[8:9], 0x0
	s_load_dwordx8 s[52:59], s[28:29], 0x0
	s_load_dwordx4 s[60:63], s[28:29], 0x20
	s_lshr_b32 s64, s3, 7
	s_lshl_b32 s65, s2, 2
	s_add_i32 s64, s64, s65
	s_ashr_i32 s65, s64, 31
	s_lshl_b64 s[64:65], s[64:65], 2
	s_add_u32 s66, s24, s64
	s_addc_u32 s67, s25, s65
	s_add_u32 s64, s26, s64
	s_addc_u32 s65, s27, s65
	s_load_dword s68, s[66:67], 0x0
	s_load_dword s69, s[64:65], 0x0
	v_lshlrev_b32_e32 v188, 2, v0
	v_add_u32_e32 v189, 0x1000, v188
	global_load_dword v184, v188, s[12:13]
	global_load_dword v185, v188, s[12:13] offset:2048
	global_load_dword v186, v189, s[12:13]
	global_load_dword v187, v189, s[12:13] offset:2048
	s_and_b32 s37, s11, 0xffff
	s_lshl_b32 s11, s3, 4
	s_mov_b32 s38, 0xf0000
	s_and_b32 s42, s11, 0xfffffc00
	s_mov_b32 s4, s10
	s_mov_b32 s5, s37
	s_mov_b32 s6, s38
	s_mov_b32 s7, s39
	v_or_b32_e32 v125, s42, v121
	s_add_i32 m0, s42, 0x1a000
	s_movk_i32 s11, 0x2000
	buffer_load_dwordx4 v125, s[4:7], 0 offen lds
	s_add_i32 m0, s42, 0x1c000
	s_nop 0
	buffer_load_dwordx4 v125, s[4:7], s11 offen lds
	s_add_i32 m0, s42, 0x1e000
	s_movk_i32 s11, 0x4000
	buffer_load_dwordx4 v125, s[4:7], s11 offen lds
	s_add_i32 m0, s42, 0x20000
	s_movk_i32 s11, 0x6000
	buffer_load_dwordx4 v125, s[4:7], s11 offen lds
	s_add_i32 m0, s42, 0x22000
	s_mov_b32 s11, 0xe8000
	buffer_load_dwordx4 v125, s[4:7], s11 offen lds
	s_lshr_b32 s70, s2, 3
	s_cmp_ge_u32 s70, 30
	s_cselect_b32 s71, 30, 0
	s_sub_u32 s70, s70, s71
	s_lshl_b32 s70, s70, 15
	v_lshlrev_b32_e32 v190, 4, v0
	buffer_load_dwordx4 v[192:195], v190, s[4:7], s70 offen
	s_add_u32 s71, s70, 0x2000
	buffer_load_dwordx4 v[196:199], v190, s[4:7], s71 offen
	s_add_u32 s72, s70, 0x4000
	buffer_load_dwordx4 v[200:203], v190, s[4:7], s72 offen
	s_add_u32 s73, s70, 0x6000
	buffer_load_dwordx4 v[204:207], v190, s[4:7], s73 offen
	s_mov_b32 s36, s10
	s_waitcnt lgkmcnt(0)
	s_mov_b32 s0, s50
	s_lshl_b32 s1, s2, 2
	s_mov_b32 s2, s51
	s_lshr_b32 s31, s3, 7
	s_bfe_u32 s30, s3, 0x10006
	s_waitcnt lgkmcnt(0)
	v_cvt_f32_i32_e32 v1, s0
	s_add_i32 s12, s31, s1
	s_add_i32 s1, s0, 0xf423f
	s_cmp_lt_u32 s1, 0x1e847f
	v_mov_b32_e32 v2, s0
	s_cselect_b64 vcc, -1, 0
	v_cndmask_b32_e32 v123, v2, v1, vcc
	v_cvt_f32_i32_e32 v1, s2
	s_add_i32 s0, s2, 0xf423f
	s_cmp_lt_u32 s0, 0x1e847f
	v_mov_b32_e32 v2, s2
	s_cselect_b64 vcc, -1, 0
	v_cndmask_b32_e32 v1, v2, v1, vcc
	v_sub_f32_e32 v122, v1, v123
	s_mov_b32 s2, 0x427c0000
	v_div_scale_f32 v1, s[0:1], s2, s2, v122
	v_rcp_f32_e32 v2, v1
	s_ashr_i32 s13, s12, 31
	s_lshl_b64 s[0:1], s[12:13], 2
	s_add_u32 s4, s24, s0
	v_fma_f32 v5, -v1, v2, 1.0
	s_addc_u32 s5, s25, s1
	v_fmac_f32_e32 v2, v5, v2
	v_div_scale_f32 v5, vcc, v122, s2, v122
	s_add_u32 s0, s26, s0
	v_mul_f32_e32 v6, v5, v2
	s_mov_b64 s[16:17], s[52:53]
	s_mov_b64 s[18:19], s[54:55]
	s_mov_b64 s[20:21], s[56:57]
	s_mov_b64 s[22:23], s[58:59]
	s_addc_u32 s1, s27, s1
	v_fma_f32 v7, -v1, v6, v5
	s_mov_b32 s4, s68
	v_fmac_f32_e32 v6, v7, v2
	s_mov_b32 s0, s69
	v_fma_f32 v1, -v1, v6, v5
	v_div_fmas_f32 v1, v1, v2, v6
	v_div_fixup_f32 v124, v1, s2, v122
	s_waitcnt lgkmcnt(0)
	v_mov_b32_e32 v1, s16
	s_mov_b64 s[24:25], s[60:61]
	s_mov_b64 s[26:27], s[62:63]
	v_mul_f32_e32 v1, s4, v1
	v_mov_b32_e32 v2, s0
	v_fma_f32 v1, s17, -v2, v1
	v_add_f32_e32 v127, s19, v1
	v_mov_b32_e32 v1, s20
	v_mul_f32_e32 v1, s4, v1
	v_fma_f32 v1, s21, -v2, v1
	v_add_f32_e32 v128, s23, v1
	s_waitcnt lgkmcnt(0)
	v_mov_b32_e32 v1, s24
	v_mul_f32_e32 v1, s4, v1
	v_and_b32_e32 v3, 15, v0
	v_fma_f32 v1, s25, -v2, v1
	v_and_b32_e32 v131, 48, v0
	v_lshl_or_b32 v0, s30, 6, v120
	v_add_f32_e32 v129, s27, v1
	v_add_u32_e32 v1, 1, v0
	v_cvt_f32_ubyte0_e32 v1, v1
	s_mov_b32 s4, 0x43010000
	s_and_b32 s19, s3, 0xffffff80
	v_div_scale_f32 v2, s[2:3], s4, s4, v1
	v_lshl_or_b32 v130, s30, 5, v3
	v_rcp_f32_e32 v3, v2
	v_lshrrev_b32_e32 v4, 4, v120
	v_cmp_eq_u32_e64 s[8:9], 2, v4
	v_cmp_eq_u32_e64 s[10:11], 1, v4
	v_fma_f32 v5, -v2, v3, 1.0
	v_fmac_f32_e32 v3, v5, v3
	v_div_scale_f32 v5, vcc, v1, s4, v1
	v_mul_f32_e32 v6, v5, v3
	v_fma_f32 v7, -v2, v6, v5
	v_fmac_f32_e32 v6, v7, v3
	v_fma_f32 v2, -v2, v6, v5
	v_div_fmas_f32 v2, v2, v3, v6
	v_div_fixup_f32 v134, v2, s4, v1
	v_add_u32_e32 v2, -1, v4
	v_cmp_gt_u32_e32 vcc, 2, v2
	v_mov_b32_e32 v2, 0x401550d3
	v_mov_b32_e32 v3, 0x436d0620
	v_cndmask_b32_e64 v5, v2, v3, s[8:9]
	v_mov_b32_e32 v6, 0x412e2e5e
	v_cmp_eq_u32_e64 s[0:1], 3, v4
	v_cndmask_b32_e64 v4, v5, v6, s[10:11]
	v_cmp_gt_u32_e64 s[2:3], 16, v120
	v_bfrev_b32_e32 v5, 34
	v_mov_b32_e32 v8, 0x41bc2043
	v_cndmask_b32_e64 v140, v4, 0.5, s[2:3]
	v_mov_b32_e32 v4, 0x40a14518
	v_cndmask_b32_e64 v7, v4, v5, s[8:9]
	v_cndmask_b32_e64 v7, v7, v8, s[10:11]
	v_mov_b32_e32 v9, 0x3f8a3f66
	v_cndmask_b32_e64 v141, v7, v9, s[2:3]
	v_cndmask_b32_e64 v7, v6, 0.5, s[8:9]
	v_cndmask_b32_e64 v6, v3, v6, s[8:9]
	v_mov_b32_e32 v10, 0x424b2ff5
	v_cndmask_b32_e64 v6, v6, 0.5, s[10:11]
	v_cndmask_b32_e64 v144, v6, v10, s[2:3]
	v_cndmask_b32_e64 v6, v5, v8, s[8:9]
	v_or_b32_e32 v0, s19, v0
	v_mov_b32_e32 v11, 0x42db7457
	v_cndmask_b32_e64 v6, v6, v9, s[10:11]
	v_lshlrev_b32_e32 v0, 2, v0
	v_cndmask_b32_e64 v7, v7, v10, s[10:11]
	v_cndmask_b32_e64 v145, v6, v11, s[2:3]
	v_cndmask_b32_e64 v6, 0, v10, s[8:9]
	v_add_u32_e32 v135, 0x15000, v0
	v_add_u32_e32 v136, 0x15800, v0
	v_cvt_f32_ubyte0_e32 v0, v130
	v_or_b32_e32 v138, 16, v130
	v_cndmask_b32_e64 v142, v7, v2, s[2:3]
	v_cndmask_b32_e64 v2, v6, v2, s[10:11]
	s_lshl_b32 s13, s31, 10
	s_lshl_b32 s44, s31, 8
	v_fma_f32 v137, v0, v124, v123
	v_cvt_f32_ubyte0_e32 v0, v138
	v_cndmask_b32_e64 v7, v8, v9, s[8:9]
	v_cndmask_b32_e64 v146, v2, v3, s[2:3]
	v_cndmask_b32_e64 v2, 0, v11, s[8:9]
	s_lshl_b32 s27, s19, 2
	s_add_i32 s13, s13, 0x12000
	s_add_i32 s44, s44, 0x16000
	v_fma_f32 v139, v0, v124, v123
	v_lshlrev_b32_e32 v0, 4, v130
	v_lshlrev_b32_e32 v1, 4, v138
	v_cndmask_b32_e64 v7, v7, v11, s[10:11]
	v_cndmask_b32_e64 v2, v2, v4, s[10:11]
	v_or_b32_e32 v126, 0x2000, v121
	s_add_i32 s23, s27, 0x15000
	s_add_i32 s28, s42, 0xa000
	s_add_i32 s29, s42, 0xc000
	s_add_i32 s33, s42, 0xe000
	s_add_i32 s34, s42, 0x10000
	s_add_i32 s35, s42, 0x2000
	s_add_i32 s40, s42, 0x8000
	s_add_i32 s41, s42, 0x6000
	s_addk_i32 s42, 0x4000
	s_sub_i32 s43, s19, 64
	v_lshl_or_b32 v132, v120, 4, s13
	v_lshl_or_b32 v133, v120, 2, s44
	s_mov_b32 s20, 1
	s_or_b64 s[4:5], s[2:3], vcc
	s_or_b64 s[6:7], s[2:3], s[10:11]
	v_cndmask_b32_e64 v143, v7, v4, s[2:3]
	s_mov_b32 s45, 0
	v_cndmask_b32_e64 v147, v2, v5, s[2:3]
	v_or_b32_e32 v148, 0x1a000, v121
	v_or_b32_e32 v149, 0x1a400, v121
	v_or_b32_e32 v150, 0x1a800, v121
	v_or_b32_e32 v151, 0x1ac00, v121
	v_or_b32_e32 v152, 0x1b000, v121
	v_or_b32_e32 v153, 0x1b400, v121
	v_or_b32_e32 v154, 0x1b800, v121
	v_or_b32_e32 v155, 0x1bc00, v121
	v_or_b32_e32 v156, 0x1c000, v121
	v_or_b32_e32 v157, 0x1c400, v121
	v_or_b32_e32 v158, 0x1c800, v121
	v_or_b32_e32 v159, 0x1cc00, v121
	v_or_b32_e32 v160, 0x1d000, v121
	v_or_b32_e32 v161, 0x1d400, v121
	v_or_b32_e32 v162, 0x1d800, v121
	v_or_b32_e32 v163, 0x1dc00, v121
	v_or_b32_e32 v164, 0x1e000, v121
	v_or_b32_e32 v165, 0x1e400, v121
	v_or_b32_e32 v166, 0x1e800, v121
	v_or_b32_e32 v167, 0x1ec00, v121
	v_or_b32_e32 v168, 0x1f000, v121
	v_or_b32_e32 v169, 0x1f400, v121
	v_or_b32_e32 v170, 0x1f800, v121
	v_or_b32_e32 v171, 0x1fc00, v121
	v_or_b32_e32 v172, 0x20000, v121
	v_or_b32_e32 v173, 0x20400, v121
	v_or_b32_e32 v174, 0x20800, v121
	v_or_b32_e32 v175, 0x20c00, v121
	v_or_b32_e32 v176, 0x21000, v121
	v_or_b32_e32 v177, 0x21400, v121
	v_or_b32_e32 v178, 0x21800, v121
	v_or_b32_e32 v179, 0x21c00, v121
	v_add_u32_e32 v180, s13, v0
	v_add_u32_e32 v181, s13, v1
	v_mov_b32_e32 v182, 0x13000
	s_waitcnt vmcnt(9)
	ds_write_b32 v188, v184
	ds_write_b32 v188, v185 offset:2048
	ds_write_b32 v188, v186 offset:4096
	ds_write_b32 v188, v187 offset:6144
	s_branch .LBB1_5
